# adds P7 partial-round block round-robin permutation across XCDs on top of P8 tail balancing
# baseline (speedup 1.0000x reference)
; #define LAS __attribute__((address_space(3)))
; template <class Epi, class Sched, bool GATHER, bool FP8>
; __device__ __forceinline__ void gemm_phase(LAS uchar* lds, const int K, const int LDA, const int LDB, const size_t kstepA, const size_t kstepB, const Sched& S, const Epi& E) {
;     ...
;     Unit cur, nxt; int ui = 0;
;     if (!S.next(0, cur)) return;
;     f32x4 acc[2][2][4][2];
; #pragma unroll
;     for (int a = 0; a < 2; ++a)
; #pragma unroll
;         for (int b = 0; b < 2; ++b)
; #pragma unroll
;             for (int m = 0; m < 4; ++m)
; #pragma unroll
;                 for (int n = 0; n < 2; ++n) acc[a][b][m][n] = (f32x4){0.f, 0.f, 0.f, 0.f};
;     bf16x8 At[4][2], B0[2][2], B1[2][2];
;     const char* cA = cur.pa; const char* cB = cur.pb;
;     if constexpr (GATHER) S.gather(cur, voA, (const LAS int*)nullptr);
;     __device__ __forceinline__ bool next(int i, pg8::Unit& u) const {
;         const int NB = __builtin_amdgcn_readfirstlane(tab[0]); const int L = i * G + c; if (L >= NB * nN) return false;
;         const int b = L / nN, pn = L - b * nN, e = __builtin_amdgcn_readfirstlane(tab[64 + b]);
;         u.pa = A; u.pb = B + (size_t)e * bexp + (size_t)pn * 256 * 128; u.row0 = b * 256; u.col0 = pn * 256; u.aux = e; u.blk = b; return true;
;     }
;     __device__ __forceinline__ void prefetch(const pg8::Unit& u, LAS uchar* buf, int wid, int lane) const {
;         { const int e = u.aux, lb = (u.blk - __builtin_amdgcn_readfirstlane(tab[8 + e])) * 256, w4 = wid & 3;
;             __builtin_amdgcn_global_load_lds((const unsigned*)(list + e * T + lb + 64 * w4 + lane), (LAS unsigned*)(buf + w4 * 256), 4, 0, 0); }
;     }
;     __device__ __forceinline__ void gather(const pg8::Unit& u, unsigned (&vo)[2][2], const LAS int* idx) const {
;         const int e = u.aux, lb = (u.blk - __builtin_amdgcn_readfirstlane(tab[8 + e])) * 256, cnt = __builtin_amdgcn_readfirstlane(tab[256 + u.blk]);
; #pragma unroll
;         for (int i = 0; i < 2; ++i) { int R, C; pg8::stage_rc((int)threadIdx.x * 16 + i * 8192, R, C);
; #pragma unroll
;             for (int h = 0; h < 2; ++h) { const int r = h * 128 + R; const int raw = idx ? idx[r] : list[e * T + lb + r]; const int tok = (r < cnt) ? raw : 0; vo[h][i] = ((unsigned)tok * (unsigned)K + (unsigned)C) * 2u; } }
;     }
.LBB0_917:
	s_or_b64 exec, exec, s[8:9]
	s_add_i32 s12, 0, 0x22000
	s_waitcnt vmcnt(4)
	v_mov_b32_e32 v2, s12
	s_waitcnt lgkmcnt(0)
	s_barrier
	ds_read_b32 v2, v2
	v_readfirstlane_b32 s20, v0
	s_waitcnt lgkmcnt(0)
	v_readfirstlane_b32 s2, v2
	s_lshl_b32 s2, s2, 4
	s_and_b32 s99, s87, 3
	s_lshl_b32 s98, s99, 6
	s_lshr_b32 s99, s87, 6
	s_lshl_b32 s99, s99, 4
	s_or_b32 s98, s98, s99
	s_bfe_u32 s99, s87, 0x10002
	s_lshl_b32 s99, s99, 3
	s_or_b32 s98, s98, s99
	s_bfe_u32 s99, s87, 0x30003
	s_or_b32 s98, s98, s99
	s_cmpk_eq_i32 s92, 0x100
	s_cselect_b32 s98, s98, s87
	s_lshr_b32 s101, s87, 7
	s_lshl_b32 s101, s101, 7
	s_and_b32 s99, s87, 7
	s_lshl_b32 s99, s99, 4
	s_or_b32 s101, s101, s99
	s_bfe_u32 s99, s87, 0x40003
	s_or_b32 s101, s101, s99
	s_cmpk_eq_i32 s92, 0x100
	s_cselect_b32 s101, s101, s87
	s_cmp_ge_i32 s98, s2
	s_cbranch_scc1 .LBB0_937
	s_add_u32 s8, s90, 0x6000000
	s_addc_u32 s9, s91, 0
	s_add_u32 s25, s90, 0x30000000
	s_addc_u32 s33, s91, 0
	s_add_u32 s10, s90, 0x2f00000
	s_addc_u32 s11, s91, 0
	s_ashr_i32 s2, s98, 31
	s_lshr_b32 s2, s2, 28
	s_add_i32 s2, s98, s2
	s_ashr_i32 s18, s2, 4
	s_lshl_b32 s3, s18, 2
	s_add_i32 s3, s12, s3
	v_mov_b32_e32 v2, s3
	ds_read2st64_b32 v[2:3], v2 offset0:1 offset1:4
	s_lshr_b32 s21, s20, 6
	s_and_b32 s2, s2, -16
	s_lshr_b32 s22, s20, 8
	s_lshl_b32 s52, s21, 10
	s_waitcnt lgkmcnt(0)
	v_readfirstlane_b32 s42, v2
	s_ashr_i32 s43, s42, 31
	s_sub_i32 s2, s98, s2
	s_lshl_b64 s[14:15], s[42:43], 23
	s_add_u32 s13, s25, s14
	s_addc_u32 s16, s33, s15
	s_ashr_i32 s3, s2, 31
	s_lshl_b64 s[14:15], s[2:3], 15
	s_add_u32 s44, s13, s14
	s_addc_u32 s45, s16, s15
	s_lshl_b32 s3, s42, 2
	s_add_i32 s3, s12, s3
	v_mov_b32_e32 v2, s3
	ds_read_b32 v2, v2 offset:32
	v_lshrrev_b32_e32 v13, 3, v0
	v_bfe_u32 v12, v0, 2, 4
	v_or_b32_e32 v4, 64, v13
	s_movk_i32 s3, 0x70
	v_and_or_b32 v195, v4, s3, v12
	s_waitcnt lgkmcnt(0)
	v_readfirstlane_b32 s3, v2
	s_sub_i32 s3, s18, s3
	s_lshl_b32 s3, s3, 8
	s_lshl_b32 s12, s42, 13
	s_add_i32 s3, s3, s12
	v_and_or_b32 v208, v13, 48, v12
	v_or_b32_e32 v4, s3, v208
	v_or_b32_e32 v209, 0x80, v208
	v_or_b32_e32 v210, 0x80, v195
	v_ashrrev_i32_e32 v5, 31, v4
	v_or_b32_e32 v6, s3, v209
	v_or_b32_e32 v8, s3, v195
	v_or_b32_e32 v10, s3, v210
	v_lshl_add_u64 v[4:5], v[4:5], 2, s[10:11]
	v_ashrrev_i32_e32 v7, 31, v6
	v_ashrrev_i32_e32 v9, 31, v8
	v_ashrrev_i32_e32 v11, 31, v10
	v_lshl_add_u64 v[6:7], v[6:7], 2, s[10:11]
	v_lshl_add_u64 v[8:9], v[8:9], 2, s[10:11]
	v_lshl_add_u64 v[10:11], v[10:11], 2, s[10:11]
	global_load_dword v14, v[4:5], off
	global_load_dword v15, v[6:7], off
	global_load_dword v16, v[8:9], off
	global_load_dword v17, v[10:11], off
	v_lshlrev_b32_e32 v4, 4, v0
	v_and_b32_e32 v5, 32, v0
	v_bitop3_b32 v4, v4, v5, 48 bitop3:0x6c
	v_and_or_b32 v5, v13, 32, v12
	v_and_b32_e32 v2, 48, v0
	s_movk_i32 s14, 0x46
	v_and_or_b32 v211, v0, 64, v4
	v_lshlrev_b32_e32 v4, 1, v5
	s_movk_i32 s3, 0xc6
	v_lshlrev_b32_e32 v5, 1, v195
	v_and_or_b32 v4, v4, s14, v2
	s_add_i32 s53, s52, 0
	v_and_b32_e32 v6, 0x80, v0
	v_mov_b32_e32 v197, 0
	v_and_or_b32 v5, v5, s3, v2
	v_lshlrev_b32_e32 v4, 7, v4
	s_add_i32 s54, s53, 0x10000
	v_mov_b32_e32 v199, v197
	v_lshlrev_b32_e32 v5, 7, v5
	v_or3_b32 v198, v4, v6, v211
	s_add_i32 s55, s53, 0x12000
	s_mov_b32 m0, s54
	s_mov_b64 s[12:13], 0x400
	v_or3_b32 v200, v5, v6, v211
	v_readfirstlane_b32 s3, v3
	v_lshl_add_u64 v[4:5], s[44:45], 0, v[198:199]
	s_add_i32 s56, s53, 0x14000
	global_load_lds_dwordx4 v198, s[44:45]
	s_mov_b32 m0, s55
	v_mov_b32_e32 v201, v197
	v_lshl_add_u64 v[4:5], v[4:5], 0, s[12:13]
	global_load_lds_dwordx4 v200, s[44:45]
	s_mov_b32 m0, s56
	v_cmp_gt_i32_e32 vcc, s3, v208
	v_lshl_add_u64 v[6:7], s[44:45], 0, v[200:201]
	s_add_i32 s57, s53, 0x16000
	global_load_lds_dwordx4 v[4:5], off
	v_lshl_add_u64 v[6:7], v[6:7], 0, s[12:13]
	s_mov_b32 m0, s57
	s_add_i32 s58, s53, 0x2000
	global_load_lds_dwordx4 v[6:7], off
	s_mov_b32 m0, s53
	s_add_i32 s59, s53, 0x4000
	s_add_i32 s60, s53, 0x6000
	s_load_dwordx2 s[14:15], s[0:1], 0x78
	s_cmp_eq_u32 s22, 1
	s_mov_b32 s46, 0
	s_cselect_b64 s[16:17], -1, 0
	s_cmp_lg_u32 s22, 1
	v_mov_b32_e32 v203, v197
	s_waitcnt vmcnt(0)
	v_mul_u32_u24_e32 v3, 0x880, v14
	v_mul_u32_u24_e32 v4, 0x880, v15
	v_cndmask_b32_e32 v3, 0, v3, vcc
	v_cmp_gt_i32_e32 vcc, s3, v209
	v_mul_u32_u24_e32 v5, 0x880, v16
	v_or_b32_e32 v196, v3, v211
	v_cndmask_b32_e32 v4, 0, v4, vcc
	v_cmp_gt_i32_e32 vcc, s3, v195
	v_mul_u32_u24_e32 v6, 0x880, v17
	global_load_lds_dwordx4 v196, s[8:9]
	v_cndmask_b32_e32 v5, 0, v5, vcc
	v_cmp_gt_i32_e32 vcc, s3, v210
	v_or_b32_e32 v202, v5, v211
	s_mov_b32 m0, s58
	v_cndmask_b32_e32 v6, 0, v6, vcc
	v_or_b32_e32 v3, v4, v211
	global_load_lds_dwordx4 v202, s[8:9]
	s_mov_b32 m0, s59
	v_or_b32_e32 v204, v6, v211
	global_load_lds_dwordx4 v3, s[8:9]
	s_mov_b32 m0, s60
	s_nop 0
	global_load_lds_dwordx4 v204, s[8:9]
	s_cbranch_scc1 .LBB0_920
	s_barrier

; template <class Epi, class Sched, bool GATHER, bool FP8>
; __device__ __forceinline__ void gemm_phase(LAS uchar* lds, const int K, const int LDA, const int LDB, const size_t kstepA, const size_t kstepB, const Sched& S, const Epi& E) {
;     ...
;         const bool has_next = S.next(ui + 1, nxt);
;         if constexpr (GATHER) { if (has_next) S.prefetch(nxt, lds + LDS_IDX + ((ui + 1) & 1) * 1024, wid, lane); }
;         E.prefetch(cur, lds + LDS_BIAS + (ui & 1) * 1024, wid, lane);
;         const char* nA = has_next ? nxt.pa : cA; const char* nB = has_next ? nxt.pb : cB;
;     __device__ __forceinline__ bool next(int i, pg8::Unit& u) const {
;         const int NB = __builtin_amdgcn_readfirstlane(tab[0]); const int L = i * G + c; if (L >= NB * nN) return false;
;         const int b = L / nN, pn = L - b * nN, e = __builtin_amdgcn_readfirstlane(tab[64 + b]);
;         u.pa = A; u.pb = B + (size_t)e * bexp + (size_t)pn * 256 * 128; u.row0 = b * 256; u.col0 = pn * 256; u.aux = e; u.blk = b; return true;
.LBB0_923:
	ds_read_b32 v2, v213
	s_add_i32 s71, s46, 1
	s_mul_i32 s2, s71, s92
	s_nop 0
	s_waitcnt lgkmcnt(0)
	v_readfirstlane_b32 s3, v2
	s_lshl_b32 s3, s3, 4
	s_add_i32 s99, s2, 0x100
	s_cmp_gt_i32 s99, s3
	s_cselect_b32 s99, s101, s98
	s_add_i32 s2, s2, s99
	s_cmp_lt_i32 s2, s3
	s_cselect_b64 s[40:41], -1, 0
	s_cmp_ge_i32 s2, s3
	s_cbranch_scc1 .LBB0_925
	s_ashr_i32 s3, s2, 31
	s_lshr_b32 s3, s3, 28
	s_add_i32 s3, s2, s3
	s_ashr_i32 s70, s3, 4
	s_lshl_b32 s26, s70, 2
	s_add_i32 s26, s26, 0
	s_add_i32 s26, s26, 0x22100
	v_mov_b32_e32 v2, s26
	ds_read_b32 v2, v2
	s_and_b32 s3, s3, -16
	s_sub_i32 s2, s2, s3
	s_waitcnt lgkmcnt(0)
	v_readfirstlane_b32 s26, v2
	s_ashr_i32 s27, s26, 31
	s_lshl_b64 s[28:29], s[26:27], 23
	s_add_u32 s27, s25, s28
	s_addc_u32 s30, s33, s29
	s_ashr_i32 s3, s2, 31
	s_lshl_b64 s[28:29], s[2:3], 15
	s_add_u32 s28, s27, s28
	s_addc_u32 s29, s30, s29
	s_lshl_b32 s72, s70, 8
	s_lshl_b32 s27, s2, 8
